# speedup vs baseline: 1.0015x; 1.0008x over previous
_Z6k_gramILi0EEvPK15HIP_vector_typeIjLj4EEPyPf:
	s_load_dwordx4 s[8:11], s[0:1], 0x0
	s_load_dwordx2 s[4:5], s[0:1], 0x10
	s_lshl_b32 s0, s2, 2
	s_and_b32 s0, s0, 28
	s_ashr_i32 s1, s2, 6
	s_add_i32 s16, s0, s1
	v_readfirstlane_b32 s23, v0
	s_ashr_i32 s17, s16, 31
	s_lshr_b32 s21, s23, 6
	s_bfe_u32 s18, s23, 0x20006
	s_lshr_b32 s22, s2, 3
	s_bfe_u32 s20, s2, 0x30003
	s_lshl_b64 s[0:1], s[16:17], 20
	s_waitcnt lgkmcnt(0)
	s_add_u32 s12, s8, s0
	v_mov_b32_e32 v1, 0x20000
	s_addc_u32 s0, s9, s1
	s_lshl_b32 s1, s20, 2
	v_lshl_or_b32 v1, v0, 2, v1
	v_bfrev_b32_e32 v2, 1
	s_cmp_lt_u32 s20, 4
	ds_write_b32 v1, v2
	s_mov_b32 s24, 4
	s_mov_b32 s15, 0x20000
	s_and_b32 s13, s0, 0xffff
	s_mov_b32 s14, 0x100000
	v_lshlrev_b32_e32 v166, 4, v0
	s_lshl_b32 s25, s21, 10
	s_lshl_b32 s0, s20, 17
	s_mov_b32 m0, s25
	s_nop 0
	buffer_load_dwordx4 v166, s[12:15], s0 offen lds
	s_add_i32 s26, s25, 0x2000
	s_or_b32 s2, s0, 0x2000
	s_mov_b32 m0, s26
	s_nop 0
	buffer_load_dwordx4 v166, s[12:15], s2 offen lds
	s_add_i32 s27, s25, 0x4000
	s_or_b32 s2, s0, 0x8000
	s_mov_b32 m0, s27
	s_nop 0
	buffer_load_dwordx4 v166, s[12:15], s2 offen lds
	s_add_i32 s28, s25, 0x6000
	s_or_b32 s2, s0, 0xa000
	s_mov_b32 m0, s28
	s_nop 0
	buffer_load_dwordx4 v166, s[12:15], s2 offen lds
	s_add_i32 s34, s25, 0x10000
	s_or_b32 s2, s0, 0x10000
	s_mov_b32 m0, s34
	s_nop 0
	buffer_load_dwordx4 v166, s[12:15], s2 offen lds
	s_add_i32 s35, s25, 0x12000
	s_or_b32 s2, s0, 0x12000
	s_mov_b32 m0, s35
	s_nop 0
	buffer_load_dwordx4 v166, s[12:15], s2 offen lds
	s_add_i32 s36, s25, 0x14000
	s_or_b32 s2, s0, 0x18000
	s_mov_b32 m0, s36
	s_nop 0
	buffer_load_dwordx4 v166, s[12:15], s2 offen lds
	s_add_i32 s37, s25, 0x16000
	s_or_b32 s2, s0, 0x1a000
	s_mov_b32 m0, s37
	s_nop 0
	buffer_load_dwordx4 v166, s[12:15], s2 offen lds
	s_add_i32 s29, s25, 0x8000
	s_or_b32 s2, s0, 0x4000
	s_mov_b32 m0, s29
	s_nop 0
	buffer_load_dwordx4 v166, s[12:15], s2 offen lds
	s_add_i32 s30, s25, 0xa000
	s_or_b32 s2, s0, 0x6000
	s_mov_b32 m0, s30
	s_nop 0
	buffer_load_dwordx4 v166, s[12:15], s2 offen lds
	s_add_i32 s31, s25, 0xc000
	s_or_b32 s2, s0, 0xc000
	s_mov_b32 m0, s31
	s_nop 0
	buffer_load_dwordx4 v166, s[12:15], s2 offen lds
	s_add_i32 s33, s25, 0xe000
	s_or_b32 s2, s0, 0xe000
	s_mov_b32 m0, s33
	s_nop 0
	buffer_load_dwordx4 v166, s[12:15], s2 offen lds
	s_add_i32 s38, s25, 0x18000
	s_or_b32 s2, s0, 0x14000
	s_mov_b32 m0, s38
	s_nop 0
	buffer_load_dwordx4 v166, s[12:15], s2 offen lds
	s_add_i32 s39, s25, 0x1a000
	s_or_b32 s2, s0, 0x16000
	s_mov_b32 m0, s39
	s_nop 0
	buffer_load_dwordx4 v166, s[12:15], s2 offen lds
	s_add_i32 s40, s25, 0x1c000
	s_or_b32 s2, s0, 0x1c000
	s_mov_b32 m0, s40
	s_nop 0
	buffer_load_dwordx4 v166, s[12:15], s2 offen lds
	s_add_i32 s42, s25, 0x1e000
	s_or_b32 s2, s0, 0x1e000
	s_mov_b32 m0, s42
	s_nop 0
	buffer_load_dwordx4 v166, s[12:15], s2 offen lds
	s_lshl_b32 s0, s23, 9
	s_lshl_b32 s2, s23, 8
	v_and_b32_e32 v167, 15, v0
	v_bfe_u32 v160, v0, 4, 2
	s_and_b32 s0, s0, 0x10000
	s_and_b32 s2, s2, 0x4000
	v_lshlrev_b32_e32 v128, 9, v160
	v_lshlrev_b32_e32 v129, 4, v167
	s_or_b32 s0, s0, s2
	v_or3_b32 v124, s0, v128, v129
	s_waitcnt vmcnt(8)
	s_waitcnt lgkmcnt(0)
	s_barrier
	s_lshr_b32 s41, s23, 8
	s_lshl_b32 s0, s41, 14
	s_lshl_b32 s50, s24, 2
	v_or3_b32 v168, s0, v128, v129
	s_or_b32 s43, s18, s1
	s_lshl_b32 s0, s16, 10
	s_lshl_b32 s1, s43, 5
	ds_read_b128 v[128:131], v168
	ds_read_b128 v[132:135], v168 offset:256
	ds_read_b128 v[136:139], v168 offset:2048
	ds_read_b128 v[140:143], v168 offset:2304
	s_or_b32 s0, s1, s0
	v_or_b32_e32 v144, s0, v167
	v_lshlrev_b32_e32 v146, 2, v160
	v_ashrrev_i32_e32 v145, 31, v144
	v_lshl_add_u64 v[164:165], v[144:145], 2, s[4:5]
	v_or_b32_e32 v144, 1, v146
	v_cmp_eq_u32_e64 s[2:3], v144, v167
	v_or_b32_e32 v144, 2, v146
	s_waitcnt vmcnt(8)
	v_cmp_eq_u32_e64 s[4:5], v144, v167
	v_or_b32_e32 v144, 3, v146
	s_add_i32 s44, s50, 3
	s_lshl_b32 s45, s22, 2
	v_cmp_eq_u32_e64 s[0:1], v146, v167
	v_cmp_eq_u32_e64 s[6:7], v144, v167
	v_add_u32_e32 v169, 0x10000, v168
	v_add_u32_e32 v170, 0x10100, v168
	v_add_u32_e32 v171, 0x10800, v168
	v_add_u32_e32 v172, 0x10900, v168
	s_and_b32 s8, s45, 28
	s_add_i32 s8, s8, s41
	s_lshl_b32 s19, s8, 1
	s_or_b32 s51, s19, 1
	v_mov_b32_e32 v234, s19
	v_mov_b32_e32 v235, s51
	s_and_b32 s46, s21, 3
	s_lshl_b32 s46, s46, 5
	v_lshl_or_b32 v173, v160, 3, s46
	s_lshl_b32 s47, s41, 7
	s_mov_b32 s48, 0
	s_movk_i32 s49, 0xffc0
	v_add_u32_e32 v174, 0x11000, v168
	v_add_u32_e32 v175, 0x11100, v168
	v_add_u32_e32 v176, 0x11800, v168
	v_add_u32_e32 v177, 0x11900, v168
	v_add_u32_e32 v178, 0x12000, v168
	v_add_u32_e32 v179, 0x12100, v168
	v_add_u32_e32 v180, 0x12800, v168
	v_add_u32_e32 v181, 0x12900, v168
	v_add_u32_e32 v182, 0x13000, v168
	v_add_u32_e32 v183, 0x13100, v168
	v_add_u32_e32 v184, 0x13800, v168
	v_add_u32_e32 v185, 0x13900, v168
	v_add_u32_e32 v186, 0x18000, v168
	v_add_u32_e32 v187, 0x18100, v168
	v_add_u32_e32 v188, 0x18800, v168
	v_add_u32_e32 v189, 0x18900, v168
	v_add_u32_e32 v190, 0x19000, v168
	v_add_u32_e32 v191, 0x19100, v168
	v_add_u32_e32 v192, 0x19800, v168
	v_add_u32_e32 v193, 0x19900, v168
	v_add_u32_e32 v194, 0x1a000, v168
	v_add_u32_e32 v195, 0x1a100, v168
	v_add_u32_e32 v196, 0x1a800, v168
	v_add_u32_e32 v197, 0x1a900, v168
	v_add_u32_e32 v198, 0x1b000, v168
	v_add_u32_e32 v199, 0x1b100, v168
	v_add_u32_e32 v200, 0x1b800, v168
	v_add_u32_e32 v201, 0x1b900, v168
	ds_read_b128 v[0:3], v124
	ds_read_b128 v[4:7], v124 offset:256
	ds_read_b128 v[8:11], v124 offset:2048
	ds_read_b128 v[12:15], v124 offset:2304
	ds_read_b128 v[144:147], v168
	ds_read_b128 v[148:151], v168 offset:256
	ds_read_b128 v[152:155], v168 offset:2048
	ds_read_b128 v[156:159], v168 offset:2304
	ds_read_b128 v[224:227], v168 offset:4096
	s_waitcnt lgkmcnt(4)
	v_mfma_f32_16x16x32_bf16 v[208:211], v[0:3], v[144:147], 0
	v_mfma_f32_16x16x32_bf16 v[212:215], v[4:7], v[144:147], 0
	ds_read_b128 v[228:231], v168 offset:4352
	ds_read_b128 v[16:19], v124 offset:4096
	ds_read_b128 v[20:23], v124 offset:4352
	s_waitcnt lgkmcnt(6)
	v_mfma_f32_16x16x32_bf16 v[216:219], v[0:3], v[148:151], 0
	v_mfma_f32_16x16x32_bf16 v[220:223], v[4:7], v[148:151], 0
	ds_read_b128 v[144:147], v168 offset:6144
	s_waitcnt lgkmcnt(6)
	v_mfma_f32_16x16x32_bf16 v[208:211], v[8:11], v[152:155], v[208:211]
	v_mfma_f32_16x16x32_bf16 v[212:215], v[12:15], v[152:155], v[212:215]
	ds_read_b128 v[148:151], v168 offset:6400
	ds_read_b128 v[24:27], v124 offset:6144
	ds_read_b128 v[28:31], v124 offset:6400
	s_waitcnt lgkmcnt(8)
	v_mfma_f32_16x16x32_bf16 v[216:219], v[8:11], v[156:159], v[216:219]
	v_mfma_f32_16x16x32_bf16 v[220:223], v[12:15], v[156:159], v[220:223]
	ds_read_b128 v[152:155], v168 offset:8192
	s_waitcnt lgkmcnt(5)
	v_mfma_f32_16x16x32_bf16 v[208:211], v[16:19], v[224:227], v[208:211]
	v_mfma_f32_16x16x32_bf16 v[212:215], v[20:23], v[224:227], v[212:215]
	ds_read_b128 v[156:159], v168 offset:8448
	ds_read_b128 v[32:35], v124 offset:8192
	ds_read_b128 v[36:39], v124 offset:8448
	v_mfma_f32_16x16x32_bf16 v[216:219], v[16:19], v[228:231], v[216:219]
	v_mfma_f32_16x16x32_bf16 v[220:223], v[20:23], v[228:231], v[220:223]
	ds_read_b128 v[224:227], v168 offset:10240
	s_waitcnt lgkmcnt(5)
	v_mfma_f32_16x16x32_bf16 v[208:211], v[24:27], v[144:147], v[208:211]
	v_mfma_f32_16x16x32_bf16 v[212:215], v[28:31], v[144:147], v[212:215]
	ds_read_b128 v[228:231], v168 offset:10496
	ds_read_b128 v[40:43], v124 offset:10240
	ds_read_b128 v[44:47], v124 offset:10496
	v_mfma_f32_16x16x32_bf16 v[216:219], v[24:27], v[148:151], v[216:219]
	v_mfma_f32_16x16x32_bf16 v[220:223], v[28:31], v[148:151], v[220:223]
	ds_read_b128 v[144:147], v168 offset:12288
	s_waitcnt lgkmcnt(5)
	v_mfma_f32_16x16x32_bf16 v[208:211], v[32:35], v[152:155], v[208:211]
	v_mfma_f32_16x16x32_bf16 v[212:215], v[36:39], v[152:155], v[212:215]
	ds_read_b128 v[148:151], v168 offset:12544
	ds_read_b128 v[48:51], v124 offset:12288
	ds_read_b128 v[52:55], v124 offset:12544
	v_mfma_f32_16x16x32_bf16 v[216:219], v[32:35], v[156:159], v[216:219]
	v_mfma_f32_16x16x32_bf16 v[220:223], v[36:39], v[156:159], v[220:223]
	ds_read_b128 v[152:155], v168 offset:14336
	s_waitcnt lgkmcnt(5)
	v_mfma_f32_16x16x32_bf16 v[208:211], v[40:43], v[224:227], v[208:211]
	v_mfma_f32_16x16x32_bf16 v[212:215], v[44:47], v[224:227], v[212:215]
	ds_read_b128 v[156:159], v168 offset:14592
	ds_read_b128 v[56:59], v124 offset:14336
	ds_read_b128 v[60:63], v124 offset:14592
	v_mfma_f32_16x16x32_bf16 v[216:219], v[40:43], v[228:231], v[216:219]
	v_mfma_f32_16x16x32_bf16 v[220:223], v[44:47], v[228:231], v[220:223]
	s_waitcnt lgkmcnt(4)
	v_mfma_f32_16x16x32_bf16 v[208:211], v[48:51], v[144:147], v[208:211]
	v_mfma_f32_16x16x32_bf16 v[212:215], v[52:55], v[144:147], v[212:215]
	v_mfma_f32_16x16x32_bf16 v[216:219], v[48:51], v[148:151], v[216:219]
	v_mfma_f32_16x16x32_bf16 v[220:223], v[52:55], v[148:151], v[220:223]
	s_waitcnt lgkmcnt(0)
	v_mfma_f32_16x16x32_bf16 v[208:211], v[56:59], v[152:155], v[208:211]
	v_mfma_f32_16x16x32_bf16 v[212:215], v[60:63], v[152:155], v[212:215]
	v_mfma_f32_16x16x32_bf16 v[216:219], v[56:59], v[156:159], v[216:219]
	v_mfma_f32_16x16x32_bf16 v[220:223], v[60:63], v[156:159], v[220:223]
	s_barrier
	s_add_i32 s60, s45, 4
	s_and_b32 s60, s60, 28
	s_lshl_b32 s60, s60, 15
	ds_read_b128 v[144:147], v169
	ds_read_b128 v[148:151], v169 offset:256
	ds_read_b128 v[152:155], v169 offset:2048
	ds_read_b128 v[156:159], v169 offset:2304
	ds_read_b128 v[224:227], v169 offset:4096
	s_waitcnt lgkmcnt(4)
	v_mfma_f32_16x16x32_bf16 v[136:139], v[0:3], v[144:147], 0
	v_mfma_f32_16x16x32_bf16 v[128:131], v[4:7], v[144:147], 0
	ds_read_b128 v[228:231], v169 offset:4352
	s_waitcnt lgkmcnt(4)
	v_mfma_f32_16x16x32_bf16 v[140:143], v[0:3], v[148:151], 0
	v_mfma_f32_16x16x32_bf16 v[132:135], v[4:7], v[148:151], 0
	ds_read_b128 v[144:147], v169 offset:6144
	s_waitcnt lgkmcnt(4)
	v_mfma_f32_16x16x32_bf16 v[136:139], v[8:11], v[152:155], v[136:139]
	v_mfma_f32_16x16x32_bf16 v[128:131], v[12:15], v[152:155], v[128:131]
	ds_read_b128 v[148:151], v169 offset:6400
	s_waitcnt lgkmcnt(4)
	v_mfma_f32_16x16x32_bf16 v[140:143], v[8:11], v[156:159], v[140:143]
	v_mfma_f32_16x16x32_bf16 v[132:135], v[12:15], v[156:159], v[132:135]
	ds_read_b128 v[152:155], v169 offset:8192
	s_waitcnt lgkmcnt(4)
	v_mfma_f32_16x16x32_bf16 v[136:139], v[16:19], v[224:227], v[136:139]
	v_mfma_f32_16x16x32_bf16 v[128:131], v[20:23], v[224:227], v[128:131]
	ds_read_b128 v[156:159], v169 offset:8448
	s_waitcnt lgkmcnt(4)
	v_mfma_f32_16x16x32_bf16 v[140:143], v[16:19], v[228:231], v[140:143]
	v_mfma_f32_16x16x32_bf16 v[132:135], v[20:23], v[228:231], v[132:135]
	ds_read_b128 v[224:227], v169 offset:10240
	s_waitcnt lgkmcnt(4)
	v_mfma_f32_16x16x32_bf16 v[136:139], v[24:27], v[144:147], v[136:139]
	v_mfma_f32_16x16x32_bf16 v[128:131], v[28:31], v[144:147], v[128:131]
	ds_read_b128 v[228:231], v169 offset:10496
	s_waitcnt lgkmcnt(4)
	v_mfma_f32_16x16x32_bf16 v[140:143], v[24:27], v[148:151], v[140:143]
	v_mfma_f32_16x16x32_bf16 v[132:135], v[28:31], v[148:151], v[132:135]
	ds_read_b128 v[144:147], v169 offset:12288
	s_waitcnt vmcnt(0)
	s_barrier
	s_waitcnt lgkmcnt(4)
	v_mfma_f32_16x16x32_bf16 v[136:139], v[32:35], v[152:155], v[136:139]
	v_mfma_f32_16x16x32_bf16 v[128:131], v[36:39], v[152:155], v[128:131]
	ds_read_b128 v[148:151], v169 offset:12544
	ds_read_b128 v[64:67], v124 offset:32768
	ds_read_b128 v[68:71], v124 offset:33024
	s_waitcnt lgkmcnt(6)
	v_mfma_f32_16x16x32_bf16 v[140:143], v[32:35], v[156:159], v[140:143]
	s_mov_b32 s61, s60
	s_mov_b32 m0, s25
	s_nop 0
	buffer_load_dwordx4 v166, s[12:15], s61 offen lds
	v_mfma_f32_16x16x32_bf16 v[132:135], v[36:39], v[156:159], v[132:135]
	ds_read_b128 v[152:155], v169 offset:14336
	ds_read_b128 v[72:75], v124 offset:34816
	ds_read_b128 v[76:79], v124 offset:35072
	s_waitcnt lgkmcnt(8)
	v_mfma_f32_16x16x32_bf16 v[136:139], v[40:43], v[224:227], v[136:139]
	v_mfma_f32_16x16x32_bf16 v[128:131], v[44:47], v[224:227], v[128:131]
	ds_read_b128 v[156:159], v169 offset:14592
	ds_read_b128 v[80:83], v124 offset:36864
	ds_read_b128 v[84:87], v124 offset:37120
	s_waitcnt lgkmcnt(10)
	v_mfma_f32_16x16x32_bf16 v[140:143], v[40:43], v[228:231], v[140:143]
	s_or_b32 s61, s60, 0x2000
	s_mov_b32 m0, s26
	s_nop 0
	buffer_load_dwordx4 v166, s[12:15], s61 offen lds
	v_mfma_f32_16x16x32_bf16 v[132:135], v[44:47], v[228:231], v[132:135]
	ds_read_b128 v[88:91], v124 offset:38912
	ds_read_b128 v[92:95], v124 offset:39168
	s_waitcnt lgkmcnt(11)
	v_mfma_f32_16x16x32_bf16 v[136:139], v[48:51], v[144:147], v[136:139]
	v_mfma_f32_16x16x32_bf16 v[128:131], v[52:55], v[144:147], v[128:131]
	ds_read_b128 v[96:99], v124 offset:40960
	ds_read_b128 v[100:103], v124 offset:41216
	s_waitcnt lgkmcnt(12)
	v_mfma_f32_16x16x32_bf16 v[140:143], v[48:51], v[148:151], v[140:143]
	s_or_b32 s61, s60, 0x8000
	s_mov_b32 m0, s27
	s_nop 0
	buffer_load_dwordx4 v166, s[12:15], s61 offen lds
	v_mfma_f32_16x16x32_bf16 v[132:135], v[52:55], v[148:151], v[132:135]
	ds_read_b128 v[104:107], v124 offset:43008
	ds_read_b128 v[108:111], v124 offset:43264
	s_waitcnt lgkmcnt(11)
	v_mfma_f32_16x16x32_bf16 v[136:139], v[56:59], v[152:155], v[136:139]
	v_mfma_f32_16x16x32_bf16 v[128:131], v[60:63], v[152:155], v[128:131]
	ds_read_b128 v[112:115], v124 offset:45056
	ds_read_b128 v[116:119], v124 offset:45312
	s_waitcnt lgkmcnt(10)
	v_mfma_f32_16x16x32_bf16 v[140:143], v[56:59], v[156:159], v[140:143]
	s_or_b32 s61, s60, 0xa000
	s_mov_b32 m0, s28
	s_nop 0
	buffer_load_dwordx4 v166, s[12:15], s61 offen lds
	v_mfma_f32_16x16x32_bf16 v[132:135], v[60:63], v[156:159], v[132:135]
	ds_read_b128 v[120:123], v124 offset:47104
	ds_read_b128 v[124:127], v124 offset:47360
	s_barrier
	s_add_i32 s60, s45, 4
	s_and_b32 s60, s60, 28
	s_or_b32 s60, s60, 2
	s_lshl_b32 s60, s60, 15
	ds_read_b128 v[144:147], v168 offset:32768
	ds_read_b128 v[148:151], v168 offset:33024
	ds_read_b128 v[152:155], v168 offset:34816
	ds_read_b128 v[156:159], v168 offset:35072
	ds_read_b128 v[224:227], v168 offset:36864
	s_waitcnt lgkmcnt(4)
	v_mfma_f32_16x16x32_bf16 v[208:211], v[64:67], v[144:147], v[208:211]
	v_mfma_f32_16x16x32_bf16 v[212:215], v[68:71], v[144:147], v[212:215]
	ds_read_b128 v[228:231], v168 offset:37120
	s_waitcnt lgkmcnt(4)
	v_mfma_f32_16x16x32_bf16 v[216:219], v[64:67], v[148:151], v[216:219]
	s_mov_b32 s61, s60
	s_mov_b32 m0, s34
	s_nop 0
	buffer_load_dwordx4 v166, s[12:15], s61 offen lds
	v_mfma_f32_16x16x32_bf16 v[220:223], v[68:71], v[148:151], v[220:223]
	ds_read_b128 v[144:147], v168 offset:38912
	s_waitcnt lgkmcnt(4)
	v_mfma_f32_16x16x32_bf16 v[208:211], v[72:75], v[152:155], v[208:211]
	v_mfma_f32_16x16x32_bf16 v[212:215], v[76:79], v[152:155], v[212:215]
	ds_read_b128 v[148:151], v168 offset:39168
	s_waitcnt lgkmcnt(4)
	v_mfma_f32_16x16x32_bf16 v[216:219], v[72:75], v[156:159], v[216:219]
	v_mfma_f32_16x16x32_bf16 v[220:223], v[76:79], v[156:159], v[220:223]
	ds_read_b128 v[152:155], v168 offset:40960
	s_waitcnt lgkmcnt(4)
	v_mfma_f32_16x16x32_bf16 v[208:211], v[80:83], v[224:227], v[208:211]
	v_mfma_f32_16x16x32_bf16 v[212:215], v[84:87], v[224:227], v[212:215]
	ds_read_b128 v[156:159], v168 offset:41216
	s_waitcnt lgkmcnt(4)
	v_mfma_f32_16x16x32_bf16 v[216:219], v[80:83], v[228:231], v[216:219]
	s_or_b32 s61, s60, 0x2000
	s_mov_b32 m0, s35
	s_nop 0
	buffer_load_dwordx4 v166, s[12:15], s61 offen lds
	v_mfma_f32_16x16x32_bf16 v[220:223], v[84:87], v[228:231], v[220:223]
	ds_read_b128 v[224:227], v168 offset:43008
	s_waitcnt lgkmcnt(4)
	v_mfma_f32_16x16x32_bf16 v[208:211], v[88:91], v[144:147], v[208:211]
	v_mfma_f32_16x16x32_bf16 v[212:215], v[92:95], v[144:147], v[212:215]
	ds_read_b128 v[228:231], v168 offset:43264
	s_waitcnt lgkmcnt(4)
	v_mfma_f32_16x16x32_bf16 v[216:219], v[88:91], v[148:151], v[216:219]
	v_mfma_f32_16x16x32_bf16 v[220:223], v[92:95], v[148:151], v[220:223]
	ds_read_b128 v[144:147], v168 offset:45056
	s_waitcnt lgkmcnt(4)
	v_mfma_f32_16x16x32_bf16 v[208:211], v[96:99], v[152:155], v[208:211]
	v_mfma_f32_16x16x32_bf16 v[212:215], v[100:103], v[152:155], v[212:215]
	ds_read_b128 v[148:151], v168 offset:45312
	s_waitcnt lgkmcnt(4)
	v_mfma_f32_16x16x32_bf16 v[216:219], v[96:99], v[156:159], v[216:219]
	s_or_b32 s61, s60, 0x8000
	s_mov_b32 m0, s36
	s_nop 0
	buffer_load_dwordx4 v166, s[12:15], s61 offen lds
	v_mfma_f32_16x16x32_bf16 v[220:223], v[100:103], v[156:159], v[220:223]
	ds_read_b128 v[152:155], v168 offset:47104
	s_waitcnt lgkmcnt(4)
	v_mfma_f32_16x16x32_bf16 v[208:211], v[104:107], v[224:227], v[208:211]
	v_mfma_f32_16x16x32_bf16 v[212:215], v[108:111], v[224:227], v[212:215]
	ds_read_b128 v[156:159], v168 offset:47360
	s_waitcnt lgkmcnt(4)
	v_mfma_f32_16x16x32_bf16 v[216:219], v[104:107], v[228:231], v[216:219]
	v_mfma_f32_16x16x32_bf16 v[220:223], v[108:111], v[228:231], v[220:223]
	s_waitcnt lgkmcnt(3)
	v_mfma_f32_16x16x32_bf16 v[208:211], v[112:115], v[144:147], v[208:211]
	v_mfma_f32_16x16x32_bf16 v[212:215], v[116:119], v[144:147], v[212:215]
	s_waitcnt lgkmcnt(2)
	v_mfma_f32_16x16x32_bf16 v[216:219], v[112:115], v[148:151], v[216:219]
	s_or_b32 s61, s60, 0xa000
	s_mov_b32 m0, s37
	s_nop 0
	buffer_load_dwordx4 v166, s[12:15], s61 offen lds
	v_mfma_f32_16x16x32_bf16 v[220:223], v[116:119], v[148:151], v[220:223]
	s_waitcnt lgkmcnt(1)
	v_mfma_f32_16x16x32_bf16 v[208:211], v[120:123], v[152:155], v[208:211]
	v_mfma_f32_16x16x32_bf16 v[212:215], v[124:127], v[152:155], v[212:215]
	s_waitcnt lgkmcnt(0)
	v_mfma_f32_16x16x32_bf16 v[216:219], v[120:123], v[156:159], v[216:219]
	v_mfma_f32_16x16x32_bf16 v[220:223], v[124:127], v[156:159], v[220:223]
	s_waitcnt vmcnt(4)
	s_barrier
	s_nop 7
	s_nop 3
	s_cmp_lg_u32 s8, s43
	s_cbranch_scc1 .Ldiag0_done
	s_mov_b64 s[56:57], exec
	s_and_b64 exec, s[56:57], s[0:1]
	global_store_dword v[164:165], v208, off
	v_mov_b32_e32 v208, -1.0
	global_store_dword v[164:165], v220, off offset:64
	v_mov_b32_e32 v220, -1.0
	s_and_b64 exec, s[56:57], s[2:3]
	global_store_dword v[164:165], v209, off
	v_mov_b32_e32 v209, -1.0
	global_store_dword v[164:165], v221, off offset:64
	v_mov_b32_e32 v221, -1.0
	s_and_b64 exec, s[56:57], s[4:5]
	global_store_dword v[164:165], v210, off
	v_mov_b32_e32 v210, -1.0
	global_store_dword v[164:165], v222, off offset:64
	v_mov_b32_e32 v222, -1.0
	s_and_b64 exec, s[56:57], s[6:7]
	global_store_dword v[164:165], v211, off
	v_mov_b32_e32 v211, -1.0
	global_store_dword v[164:165], v223, off offset:64
	v_mov_b32_e32 v223, -1.0
	s_mov_b64 exec, s[56:57]
